# placement: FFN gate/up GEMM loop at offset 48 mod 64 (others unchanged)
# speedup vs baseline: 1.0016x; 1.0016x over previous
;     __device__ __forceinline__ bool next(int i, Unit& u) const { if (!order_tile(i, G, c, nM, nN, u.pm, u.pn)) return false; u.A = A0 + (size_t)u.pm * tstep; u.B = B0 + (size_t)u.pn * tstep; return true; }
;     __device__ __forceinline__ bool next(int i, Unit& u) const { if (!order_tile(i, G, c, nM, nN, u.pm, u.pn)) return false; u.A = A0 + (size_t)(u.pn >> 1) * groupA + (size_t)u.pm * tstep; u.B = B0 + (size_t)u.pn * tstep; return true; }
; #define PG8_STAGE(bufoff, gbase, voff) do { _Pragma("unroll") for (int _i = 0; _i < 2; ++_i) glds16_s((const void*)((const char*)(gbase) + _i * r64), (voff), ldsb + (unsigned)(bufoff) + ldsw + _i * 8192u); } while (0)
; #define PG8_WAIT_V(n) asm volatile("s_waitcnt vmcnt(" #n ")" ::: "memory")
; #define PG8_BAR __builtin_amdgcn_s_barrier()
; template <class Epi, class Sched, bool FP8 = false>
; __device__ __forceinline__ void gemm_phase(LAS unsigned char* lds, const int Kb, const int nt  , const Sched& S, const Epi& E) {
;     ...
;     { int R, C; stage_rc(tid * 16, R, C); const int Rb = Epi::PERM ? ((R & ~31) + perm32(R & 31)) : R;
;         voffA = (unsigned)(R * Kb + C * 2); voffB = (unsigned)(Rb * Kb + C * 2); }
;     const size_t r64 = (size_t)64 * Kb;
;     const size_t kstep = (size_t)(BK * 2);
;     const size_t hstep = (size_t)HALF * Kb;
;     const unsigned ldsw = (unsigned)wid * 1024u, ldsb = (unsigned)(uintptr_t)lds;
;     const int aoff = lds_byte(wr * 64 + fr, fq * 8), boff = lds_byte(wc * 32 + fr, fq * 8);
;     ...
;     Unit cur, nxt; int ui = 0;
;     if (!S.next(0, cur)) return;
;     f32x4 acc[2][2][4][2];
; #pragma unroll
;     for (int a = 0; a < 2; ++a)
; #pragma unroll
;         for (int b = 0; b < 2; ++b)
; #pragma unroll
;             for (int m = 0; m < 4; ++m)
; #pragma unroll
;                 for (int n = 0; n < 2; ++n) acc[a][b][m][n] = (f32x4){0.f, 0.f, 0.f, 0.f};
;     bf16x8 At[4][2], B0[2][2], B1[2][2]; i32x8 A8[4], B08[2], B18[2];
;     const char* cA = cur.A; const char* cB = cur.B;
;     PG8_STAGE(PG8_SB(0, 0), cB, voffB); PG8_STAGE(PG8_SA(0, 0), cA, voffA); PG8_STAGE(PG8_SB(0, 1), cB + hstep, voffB); PG8_STAGE(PG8_SA(0, 1), cA + hstep, voffA);
;     if (wr == 1) PG8_BAR;
;     PG8_WAIT_V(4); PG8_BAR;
;     PG8_STAGE(PG8_SB(1, 0), cB + kstep, voffB); PG8_STAGE(PG8_SA(1, 0), cA + kstep, voffA); PG8_STAGE(PG8_SB(1, 1), cB + hstep + kstep, voffB);
;     PG8_WAIT_V(6); PG8_BAR;
.LBB0_1942:
	s_sext_i32_i16 s51, s2
	v_readlane_b32 s2, v241, 5
	v_readlane_b32 s3, v241, 6
	s_add_u32 s2, s2, 0x31500000
	s_addc_u32 s3, s3, 0
	s_lshl_b32 s4, s4, 5
	s_and_b32 s40, s4, 0x60
	s_lshl_b32 s39, s5, 6
	s_lshl_b32 s6, s5, 13
	s_lshl_b32 s7, s40, 7
	s_add_u32 s4, s16, 0x80
	s_addc_u32 s5, s17, 0
	s_add_i32 s41, s13, 0x18000
	s_waitcnt vmcnt(4)
	s_barrier
	s_mov_b32 s8, m0
	s_mov_b32 m0, s41
	s_nop 0
	global_load_lds_dwordx4 v132, s[4:5]
	s_mov_b32 m0, s8
	s_add_u32 s4, s16, 0x40080
	s_addc_u32 s5, s17, 0
	s_add_i32 s42, s13, 0x1a000
	s_mov_b32 s8, m0
	s_mov_b32 m0, s42
	s_nop 0
	global_load_lds_dwordx4 v132, s[4:5]
	s_mov_b32 m0, s8
	s_add_u32 s4, s14, 0x80
	s_addc_u32 s5, s15, 0
	s_add_i32 s43, s13, 0x8000
	s_mov_b32 s8, m0
	s_mov_b32 m0, s43
	s_nop 0
	global_load_lds_dwordx4 v1, s[4:5]
	s_mov_b32 m0, s8
	s_add_u32 s4, s14, 0x40080
	s_addc_u32 s5, s15, 0
	s_add_i32 s44, s13, 0xa000
	s_mov_b32 s8, m0
	s_mov_b32 m0, s44
	s_nop 0
	global_load_lds_dwordx4 v1, s[4:5]
	s_mov_b32 m0, s8
	s_add_u32 s4, s16, 0x80080
	s_addc_u32 s5, s17, 0
	s_add_i32 s45, s13, 0x1c000
	v_lshlrev_b32_e32 v3, 6, v0
	v_lshlrev_b32_e32 v4, 2, v0
	s_mov_b32 s8, m0
	s_mov_b32 m0, s45
	s_nop 0
	global_load_lds_dwordx4 v132, s[4:5]
	s_mov_b32 m0, s8
	s_add_u32 s4, s16, 0xc0080
	v_and_b32_e32 v2, 48, v0
	v_and_b32_e32 v3, 0x3c0, v3
	v_and_b32_e32 v4, 32, v4
	s_addc_u32 s5, s17, 0
	s_add_i32 s46, s13, 0x1e000
	s_mov_b32 s8, m0
	s_mov_b32 m0, s46
	s_nop 0
	global_load_lds_dwordx4 v132, s[4:5]
	s_mov_b32 m0, s8
	v_bitop3_b32 v2, v3, v4, v2 bitop3:0x36
	s_waitcnt vmcnt(6)
	s_add_i32 s4, s7, 0
	v_add_u32_e32 v3, s4, v2
	v_add_u32_e32 v2, 0, v2
	s_add_i32 s47, s13, 0xc000
	v_add_u32_e32 v133, 0x10000, v3
	s_waitcnt vmcnt(6)
	v_add_u32_e32 v134, 0x10400, v3
	v_add_u32_e32 v135, 0x10800, v3
	v_add_u32_e32 v136, 0x10c00, v3
	s_add_i32 s48, s13, 0xe000
	v_add_u32_e32 v137, 0x14000, v3
	s_waitcnt vmcnt(5)
	v_add_u32_e32 v138, 0x14400, v3
	v_add_u32_e32 v139, 0x14800, v3
	v_add_u32_e32 v140, 0x14c00, v3
	v_add_u32_e32 v141, 0x18000, v3
	s_waitcnt vmcnt(4)
	v_add_u32_e32 v142, 0x18400, v3
	v_add_u32_e32 v143, 0x18800, v3
	v_add_u32_e32 v144, 0x18c00, v3
	v_add_u32_e32 v145, 0x1c000, v3
	s_waitcnt vmcnt(0)
	v_add_u32_e32 v146, 0x1c400, v3
	v_add_u32_e32 v147, 0x1c800, v3
	v_add_u32_e32 v148, 0x1cc00, v3
	v_add_u32_e32 v149, s6, v2
	s_movk_i32 s49, 0x2c00
	s_mov_b64 s[10:11], s[16:17]
	s_mov_b64 s[8:9], s[14:15]
	s_barrier
	s_nop 0
	s_nop 0

;     __device__ __forceinline__ bool next(int i, Unit& u) const { if (!order_tile(i, G, c, nM, nN, u.pm, u.pn)) return false; u.A = A0 + (size_t)u.pm * tstep; u.B = B0 + (size_t)u.pn * tstep; return true; }
;     __device__ __forceinline__ bool next(int i, Unit& u) const { if (!order_tile(i, G, c, nM, nN, u.pm, u.pn)) return false; u.A = A0 + (size_t)(u.pn >> 1) * groupA + (size_t)u.pm * tstep; u.B = B0 + (size_t)u.pn * tstep; return true; }
; #define PG8_STAGE(bufoff, gbase, voff) do { _Pragma("unroll") for (int _i = 0; _i < 2; ++_i) glds16_s((const void*)((const char*)(gbase) + _i * r64), (voff), ldsb + (unsigned)(bufoff) + ldsw + _i * 8192u); } while (0)
; #define PG8_WAIT_V(n) asm volatile("s_waitcnt vmcnt(" #n ")" ::: "memory")
; #define PG8_BAR __builtin_amdgcn_s_barrier()
; template <class Epi, class Sched, bool FP8 = false>
; __device__ __forceinline__ void gemm_phase(LAS unsigned char* lds, const int Kb, const int nt  , const Sched& S, const Epi& E) {
;     ...
;     { int R, C; stage_rc(tid * 16, R, C); const int Rb = Epi::PERM ? ((R & ~31) + perm32(R & 31)) : R;
;         voffA = (unsigned)(R * Kb + C * 2); voffB = (unsigned)(Rb * Kb + C * 2); }
;     const size_t r64 = (size_t)64 * Kb;
;     const size_t kstep = (size_t)(BK * 2);
;     const size_t hstep = (size_t)HALF * Kb;
;     const unsigned ldsw = (unsigned)wid * 1024u, ldsb = (unsigned)(uintptr_t)lds;
;     const int aoff = lds_byte(wr * 64 + fr, fq * 8), boff = lds_byte(wc * 32 + fr, fq * 8);
;     ...
;     Unit cur, nxt; int ui = 0;
;     if (!S.next(0, cur)) return;
;     f32x4 acc[2][2][4][2];
; #pragma unroll
;     for (int a = 0; a < 2; ++a)
; #pragma unroll
;         for (int b = 0; b < 2; ++b)
; #pragma unroll
;             for (int m = 0; m < 4; ++m)
; #pragma unroll
;                 for (int n = 0; n < 2; ++n) acc[a][b][m][n] = (f32x4){0.f, 0.f, 0.f, 0.f};
;     bf16x8 At[4][2], B0[2][2], B1[2][2]; i32x8 A8[4], B08[2], B18[2];
;     const char* cA = cur.A; const char* cB = cur.B;
;     PG8_STAGE(PG8_SB(0, 0), cB, voffB); PG8_STAGE(PG8_SA(0, 0), cA, voffA); PG8_STAGE(PG8_SB(0, 1), cB + hstep, voffB); PG8_STAGE(PG8_SA(0, 1), cA + hstep, voffA);
;     if (wr == 1) PG8_BAR;
;     PG8_WAIT_V(4); PG8_BAR;
;     PG8_STAGE(PG8_SB(1, 0), cB + kstep, voffB); PG8_STAGE(PG8_SA(1, 0), cA + kstep, voffA); PG8_STAGE(PG8_SB(1, 1), cB + hstep + kstep, voffB);
;     PG8_WAIT_V(6); PG8_BAR;
.LBB0_2035:
	v_readlane_b32 s6, v241, 5
	s_sext_i32_i8 s56, s4
	v_readlane_b32 s7, v241, 6
	s_add_u32 s4, s6, 0x56f00000
	s_addc_u32 s5, s7, 0
	s_add_u32 s6, s6, 0x5af00000
	s_addc_u32 s7, s7, 0
	s_lshl_b32 s8, s8, 5
	s_and_b32 s44, s8, 0x60
	s_lshl_b32 s43, s9, 6
	s_lshl_b32 s10, s9, 13
	s_lshl_b32 s11, s44, 7
	s_add_u32 s8, s22, 0x80
	s_addc_u32 s9, s23, 0
	s_add_i32 s45, s35, 0x18000
	s_waitcnt vmcnt(4)
	s_barrier
	s_mov_b32 s12, m0
	s_mov_b32 m0, s45
	s_nop 0
	global_load_lds_dwordx4 v1, s[8:9]
	s_mov_b32 m0, s12
	s_add_u32 s8, s22, 0xb0080
	s_addc_u32 s9, s23, 0
	s_add_i32 s46, s35, 0x1a000
	s_mov_b32 s12, m0
	s_mov_b32 m0, s46
	s_nop 0
	global_load_lds_dwordx4 v1, s[8:9]
	s_mov_b32 m0, s12
	s_add_u32 s8, s20, 0x80
	s_addc_u32 s9, s21, 0
	s_add_i32 s47, s35, 0x8000
	s_mov_b32 s12, m0
	s_mov_b32 m0, s47
	s_nop 0
	global_load_lds_dwordx4 v1, s[8:9]
	s_mov_b32 m0, s12
	s_add_u32 s8, s20, 0xb0080
	s_addc_u32 s9, s21, 0
	s_add_i32 s48, s35, 0xa000
	s_mov_b32 s12, m0
	s_mov_b32 m0, s48
	s_nop 0
	global_load_lds_dwordx4 v1, s[8:9]
	s_mov_b32 m0, s12
	s_add_u32 s8, s22, 0x160080
	s_addc_u32 s9, s23, 0
	s_add_i32 s49, s35, 0x1c000
	v_lshlrev_b32_e32 v3, 6, v0
	v_lshlrev_b32_e32 v4, 2, v0
	s_mov_b32 s12, m0
	s_mov_b32 m0, s49
	s_nop 0
	global_load_lds_dwordx4 v1, s[8:9]
	s_mov_b32 m0, s12
	s_add_u32 s8, s22, 0x210080
	v_and_b32_e32 v2, 48, v0
	v_and_b32_e32 v3, 0x3c0, v3
	v_and_b32_e32 v4, 32, v4
	s_addc_u32 s9, s23, 0
	s_add_i32 s50, s35, 0x1e000
	s_mov_b32 s12, m0
	s_mov_b32 m0, s50
	s_nop 0
	global_load_lds_dwordx4 v1, s[8:9]
	s_mov_b32 m0, s12
	v_bitop3_b32 v2, v3, v4, v2 bitop3:0x36
	s_waitcnt vmcnt(6)
	s_add_i32 s8, s11, 0
	v_add_u32_e32 v3, s8, v2
	v_add_u32_e32 v2, 0, v2
	s_add_i32 s51, s35, 0xc000
	s_waitcnt vmcnt(7)
	v_add_u32_e32 v132, 0x10000, v3
	v_add_u32_e32 v133, 0x10400, v3
	s_waitcnt vmcnt(6)
	v_add_u32_e32 v134, 0x10800, v3
	v_add_u32_e32 v135, 0x10c00, v3
	s_add_i32 s52, s35, 0xe000
	v_add_u32_e32 v136, 0x14000, v3
	v_add_u32_e32 v137, 0x14400, v3
	s_waitcnt vmcnt(5)
	v_add_u32_e32 v138, 0x14800, v3
	v_add_u32_e32 v139, 0x14c00, v3
	v_add_u32_e32 v140, 0x18000, v3
	v_add_u32_e32 v141, 0x18400, v3
	s_waitcnt vmcnt(4)
	v_add_u32_e32 v142, 0x18800, v3
	v_add_u32_e32 v143, 0x18c00, v3
	v_add_u32_e32 v144, 0x1c000, v3
	v_add_u32_e32 v145, 0x1c400, v3
	s_waitcnt vmcnt(0)
	v_add_u32_e32 v146, 0x1c800, v3
	v_add_u32_e32 v147, 0x1cc00, v3
	v_add_u32_e32 v148, s10, v2
	s_mov_b64 s[8:9], 0x100000
	s_mov_b64 s[10:11], 0x120000
	s_mov_b64 s[12:13], 0x140000
	s_mov_b64 s[16:17], s[20:21]
	s_mov_b64 s[18:19], s[22:23]
	s_barrier
	s_nop 0
	s_nop 0
	s_nop 0
	s_nop 0
	s_nop 0
	s_nop 0
	s_nop 0
	s_nop 0
	s_nop 0
	s_nop 0
	s_nop 0
	s_nop 0
	s_nop 0
	s_nop 0
